# P3 GLA scan: one static s_setprio 1 for the compute waves (0-4) over the load-only waves sharing their SIMDs
# speedup vs baseline: 1.0088x; 1.0022x over previous
; #define REP(k) for (int rep_ = 0; rep_ < ((PROBE_DUP) == (k) ? 2 : 1); ++rep_)
; #define SEAM(k) do { if (IN(k) && IN((k) + 1)) xcd_barrier(bar); } while (0)
; __device__ __forceinline__ void gla_scan_chain(Frame& F, int chain) {
;     ...
;     asm volatile("s_waitcnt vmcnt(0) lgkmcnt(0)" ::: "memory");
; __global__ void __launch_bounds__(NTHREADS, 2) hymba_fwd(Args args) {
;     ...
;     if (IN(3)) REP(3) { for (int c = F.bid; c < 256; c += F.G) { const int cc = (F.G == 256) ? (((c & 7) * 2 + (c >> 7)) << 4) | ((c >> 3) & 15) : c; gla_scan_chain(F, cc); } } SEAM(3);
.LBB0_344:
	s_setprio 0
	s_waitcnt vmcnt(0) lgkmcnt(0)
	s_add_i32 s66, s66, s90
	s_cmpk_lt_i32 s66, 0x100
	s_cbranch_scc0 .LBB0_415

; #define LAS __attribute__((address_space(3)))
; __device__ __forceinline__ void gla_scan_chain(Frame& F, int chain) {
;     const int bh = chain >> 4, et = chain & 15, b = bh >> 3, h = bh & 7, lane = F.lane, fr = lane & 15, fq = lane >> 4, wave = F.wave;
;     bf16_t* ORAW = (bf16_t*)(F.ws + WS_ORAW);
;     f32x4 S[8];
; #pragma unroll
;     for (int i = 0; i < 8; ++i) S[i] = (f32x4){0.f, 0.f, 0.f, 0.f};
;     if (wave >= 1) { gs_load(F, bh, et, 0, 0); gs_load(F, bh, et, 1, 1); gs_wait_older(wave, true); }
;     if (wave == 0) { for (int i = lane; i < GS_SBBUF / 16; i += 64) *(LAS u32x4*)(F.lds + GS_SB + i * 16) = (u32x4){0u, 0u, 0u, 0u}; }
;     asm volatile("s_waitcnt lgkmcnt(0)" ::: "memory"); __builtin_amdgcn_s_barrier(); asm volatile("" ::: "memory");
; #pragma unroll 1
;     for (int n = 0; n < 128; ++n) {
;     ...
;         if (wave >= 1) { if (n + 2 < 128) gs_wait_older(wave, false); else asm volatile("s_waitcnt vmcnt(0)" ::: "memory"); }
;         asm volatile("s_waitcnt lgkmcnt(0)" ::: "memory"); __builtin_amdgcn_s_barrier(); asm volatile("" ::: "memory");
;     }
.LBB0_359:
	s_lshl_b32 s34, s18, 7
	s_ashr_i32 s29, s28, 31
	s_and_b32 s18, s30, 15
	s_lshl_b32 s30, s30, 5
	s_waitcnt lgkmcnt(0)
	s_barrier
	s_and_b32 s35, s30, 0xe00
	s_lshl_b64 s[28:29], s[28:29], 25
	v_mov_b32_e32 v4, v2
	v_mov_b32_e32 v5, v2
	s_or_b32 s30, s67, s35
	s_or_b32 s28, s28, s35
	v_mov_b32_e32 v3, v2
	v_mov_b64_e32 v[12:13], v[4:5]
	v_mov_b64_e32 v[16:17], v[4:5]
	v_mov_b64_e32 v[20:21], v[4:5]
	v_mov_b64_e32 v[24:25], v[4:5]
	v_mov_b64_e32 v[28:29], v[4:5]
	v_mov_b64_e32 v[32:33], v[4:5]
	v_mov_b64_e32 v[36:37], v[4:5]
	v_mov_b64_e32 v[40:41], v[4:5]
	s_lshl_b32 s18, s18, 5
	v_lshl_add_u64 v[88:89], v[84:85], 0, s[30:31]
	s_or_b32 s36, s34, 2
	v_lshl_add_u64 v[90:91], v[86:87], 0, s[28:29]
	s_mov_b32 s37, 0
	v_mov_b64_e32 v[10:11], v[2:3]
	v_mov_b64_e32 v[14:15], v[2:3]
	v_mov_b64_e32 v[18:19], v[2:3]
	v_mov_b64_e32 v[22:23], v[2:3]
	v_mov_b64_e32 v[26:27], v[2:3]
	v_mov_b64_e32 v[30:31], v[2:3]
	v_mov_b64_e32 v[34:35], v[2:3]
	v_mov_b64_e32 v[38:39], v[2:3]
	s_and_b64 vcc, exec, s[10:11]
	s_cbranch_vccz .Lgs_noprio
	s_setprio 1
.Lgs_noprio:
	s_branch .LBB0_361
.LBB0_360:
	s_waitcnt lgkmcnt(0)
	s_barrier
	s_mov_b64 s[28:29], 0x118000
	s_add_i32 s37, s37, 1
	v_lshl_add_u64 v[88:89], v[88:89], 0, s[28:29]
	s_mov_b64 s[28:29], 0x40000
	s_cmpk_lg_i32 s37, 0x80
	v_lshl_add_u64 v[90:91], v[90:91], 0, s[28:29]
	s_cbranch_scc0 .LBB0_344
